# combined variant plus non-temporal stores in the expert down-projection (P10) epilogue
# speedup vs baseline: 1.0100x; 1.0100x over previous
.LBB0_1473:
	v_mov_b32_e32 v19, v187
	v_mov_b32_e32 v17, v186
	s_nop 15
	s_nop 15
	v_pk_mul_f32 v[24:25], v[140:141], s[30:31] op_sel_hi:[1,0]
	v_lshl_add_u32 v18, v17, 4, v19
	v_ashrrev_i32_e32 v18, 2, v18
	v_and_b32_e32 v20, 3, v19
	v_mul_lo_u32 v21, v19, s71
	v_lshlrev_b32_e32 v17, 3, v17
	v_add3_u32 v17, s68, v21, v17
	v_mul_lo_u32 v21, v18, s71
	v_lshlrev_b32_e32 v20, 4, v20
	v_add3_u32 v22, s68, v21, v20
	v_lshlrev_b32_e32 v20, 6, v19
	v_and_b32_e32 v180, 0x80, v20
	v_pk_mul_f32 v[20:21], v[136:137], s[30:31] op_sel_hi:[1,0]
	v_mov_b32_e32 v26, v181
	v_mov_b32_e32 v27, v181
	v_cvt_pk_fp8_f32 v26, v20, v21
	v_cvt_pk_fp8_f32 v27, v24, v25
	v_pk_mul_f32 v[20:21], v[138:139], s[30:31] op_sel_hi:[1,0]
	v_pk_mul_f32 v[24:25], v[142:143], s[30:31] op_sel_hi:[1,0]
	v_cvt_pk_fp8_f32 v26, v20, v21 op_sel:[0,0,1]
	v_cvt_pk_fp8_f32 v27, v24, v25 op_sel:[0,0,1]
	v_pk_mul_f32 v[20:21], v[160:161], s[30:31] op_sel_hi:[1,0]
	v_pk_mul_f32 v[24:25], v[164:165], s[30:31] op_sel_hi:[1,0]
	v_mov_b32_e32 v28, v181
	v_mov_b32_e32 v29, v181
	v_cvt_pk_fp8_f32 v28, v20, v21
	v_cvt_pk_fp8_f32 v29, v24, v25
	v_pk_mul_f32 v[30:31], v[120:121], s[30:31] op_sel_hi:[1,0]
	v_pk_mul_f32 v[32:33], v[124:125], s[30:31] op_sel_hi:[1,0]
	v_mov_b32_e32 v34, v181
	v_mov_b32_e32 v35, v181
	v_cvt_pk_fp8_f32 v34, v30, v31
	v_cvt_pk_fp8_f32 v35, v32, v33
	s_lshl_b32 s6, s42, 8
	v_pk_mul_f32 v[20:21], v[162:163], s[30:31] op_sel_hi:[1,0]
	v_pk_mul_f32 v[24:25], v[166:167], s[30:31] op_sel_hi:[1,0]
	s_add_i32 s6, s6, s65
	v_cvt_pk_fp8_f32 v28, v20, v21 op_sel:[0,0,1]
	v_cvt_pk_fp8_f32 v29, v24, v25 op_sel:[0,0,1]
	v_pk_mul_f32 v[30:31], v[122:123], s[30:31] op_sel_hi:[1,0]
	v_pk_mul_f32 v[32:33], v[126:127], s[30:31] op_sel_hi:[1,0]
	v_add_u32_e32 v18, s6, v18
	v_lshlrev_b32_e32 v19, 4, v19
	v_cvt_pk_fp8_f32 v34, v30, v31 op_sel:[0,0,1]
	v_cvt_pk_fp8_f32 v35, v32, v33 op_sel:[0,0,1]
	v_pk_mul_f32 v[30:31], v[144:145], s[30:31] op_sel_hi:[1,0]
	v_pk_mul_f32 v[32:33], v[152:153], s[30:31] op_sel_hi:[1,0]
	v_mov_b32_e32 v36, v181
	v_mov_b32_e32 v37, v181
	v_and_b32_e32 v20, 16, v19
	v_ashrrev_i32_e32 v19, 31, v18
	v_cvt_pk_fp8_f32 v36, v30, v31
	v_cvt_pk_fp8_f32 v37, v32, v33
	s_lshl_b32 s6, s44, 8
	ds_write_b64 v17, v[26:27]
	ds_write_b64 v17, v[28:29] offset:32
	v_lshlrev_b64 v[28:29], 11, v[18:19]
	s_ashr_i32 s7, s6, 31
	ds_read_b128 v[24:27], v22
	v_lshl_add_u64 v[28:29], s[20:21], 0, v[28:29]
	v_lshl_add_u64 v[28:29], v[28:29], 0, s[6:7]
	v_pk_mul_f32 v[30:31], v[146:147], s[30:31] op_sel_hi:[1,0]
	v_pk_mul_f32 v[32:33], v[154:155], s[30:31] op_sel_hi:[1,0]
	v_lshl_add_u64 v[28:29], v[28:29], 0, v[180:181]
	v_cvt_pk_fp8_f32 v36, v30, v31 op_sel:[0,0,1]
	v_cvt_pk_fp8_f32 v37, v32, v33 op_sel:[0,0,1]
	v_mov_b32_e32 v21, v181
	v_lshl_add_u64 v[28:29], v[28:29], 0, s[18:19]
	v_lshl_add_u64 v[28:29], v[28:29], 0, v[20:21]
	s_waitcnt lgkmcnt(0)
	global_store_dwordx4 v[28:29], v[24:27], off nt
	ds_write_b64 v17, v[34:35]
	ds_write_b64 v17, v[36:37] offset:32
	v_pk_mul_f32 v[30:31], v[96:97], s[30:31] op_sel_hi:[1,0]
	v_pk_mul_f32 v[32:33], v[100:101], s[30:31] op_sel_hi:[1,0]
	v_mov_b32_e32 v34, v181
	v_mov_b32_e32 v35, v181
	v_cvt_pk_fp8_f32 v34, v30, v31
	v_cvt_pk_fp8_f32 v35, v32, v33
	v_pk_mul_f32 v[30:31], v[98:99], s[30:31] op_sel_hi:[1,0]
	v_pk_mul_f32 v[32:33], v[102:103], s[30:31] op_sel_hi:[1,0]
	v_add_u32_e32 v28, 16, v18
	v_cvt_pk_fp8_f32 v34, v30, v31 op_sel:[0,0,1]
	v_cvt_pk_fp8_f32 v35, v32, v33 op_sel:[0,0,1]
	v_pk_mul_f32 v[30:31], v[128:129], s[30:31] op_sel_hi:[1,0]
	v_pk_mul_f32 v[32:33], v[132:133], s[30:31] op_sel_hi:[1,0]
	v_mov_b32_e32 v36, v181
	v_mov_b32_e32 v37, v181
	v_ashrrev_i32_e32 v29, 31, v28
	v_cvt_pk_fp8_f32 v36, v30, v31
	v_cvt_pk_fp8_f32 v37, v32, v33
	v_lshlrev_b64 v[28:29], 11, v[28:29]
	ds_read_b128 v[24:27], v22
	v_lshl_add_u64 v[28:29], s[20:21], 0, v[28:29]
	v_lshl_add_u64 v[28:29], v[28:29], 0, s[6:7]
	v_pk_mul_f32 v[30:31], v[130:131], s[30:31] op_sel_hi:[1,0]
	v_pk_mul_f32 v[32:33], v[134:135], s[30:31] op_sel_hi:[1,0]
	v_lshl_add_u64 v[28:29], v[28:29], 0, v[180:181]
	v_cvt_pk_fp8_f32 v36, v30, v31 op_sel:[0,0,1]
	v_cvt_pk_fp8_f32 v37, v32, v33 op_sel:[0,0,1]
	v_lshl_add_u64 v[28:29], v[28:29], 0, s[18:19]
	v_lshl_add_u64 v[28:29], v[28:29], 0, v[20:21]
	s_waitcnt lgkmcnt(0)
	global_store_dwordx4 v[28:29], v[24:27], off nt
	ds_write_b64 v17, v[34:35]
	ds_write_b64 v17, v[36:37] offset:32
	v_pk_mul_f32 v[30:31], v[80:81], s[30:31] op_sel_hi:[1,0]
	v_pk_mul_f32 v[32:33], v[84:85], s[30:31] op_sel_hi:[1,0]
	v_mov_b32_e32 v34, v181
	v_mov_b32_e32 v35, v181
	v_cvt_pk_fp8_f32 v34, v30, v31
	v_cvt_pk_fp8_f32 v35, v32, v33
	v_pk_mul_f32 v[30:31], v[82:83], s[30:31] op_sel_hi:[1,0]
	v_pk_mul_f32 v[32:33], v[86:87], s[30:31] op_sel_hi:[1,0]
	v_add_u32_e32 v28, 32, v18
	v_cvt_pk_fp8_f32 v34, v30, v31 op_sel:[0,0,1]
	v_cvt_pk_fp8_f32 v35, v32, v33 op_sel:[0,0,1]
	v_pk_mul_f32 v[30:31], v[104:105], s[30:31] op_sel_hi:[1,0]
	v_pk_mul_f32 v[32:33], v[112:113], s[30:31] op_sel_hi:[1,0]
	v_mov_b32_e32 v36, v181
	v_mov_b32_e32 v37, v181
	v_ashrrev_i32_e32 v29, 31, v28
	v_cvt_pk_fp8_f32 v36, v30, v31
	v_cvt_pk_fp8_f32 v37, v32, v33
	v_lshlrev_b64 v[28:29], 11, v[28:29]
	ds_read_b128 v[24:27], v22
	v_lshl_add_u64 v[28:29], s[20:21], 0, v[28:29]
	v_lshl_add_u64 v[28:29], v[28:29], 0, s[6:7]
	v_pk_mul_f32 v[30:31], v[106:107], s[30:31] op_sel_hi:[1,0]
	v_pk_mul_f32 v[32:33], v[114:115], s[30:31] op_sel_hi:[1,0]
	v_lshl_add_u64 v[28:29], v[28:29], 0, v[180:181]
	v_cvt_pk_fp8_f32 v36, v30, v31 op_sel:[0,0,1]
	v_cvt_pk_fp8_f32 v37, v32, v33 op_sel:[0,0,1]
	v_lshl_add_u64 v[28:29], v[28:29], 0, s[18:19]
	v_lshl_add_u64 v[28:29], v[28:29], 0, v[20:21]
	s_waitcnt lgkmcnt(0)
	global_store_dwordx4 v[28:29], v[24:27], off nt
	ds_write_b64 v17, v[34:35]
	ds_write_b64 v17, v[36:37] offset:32
	v_pk_mul_f32 v[30:31], v[108:109], s[30:31] op_sel_hi:[1,0]
	v_pk_mul_f32 v[32:33], v[116:117], s[30:31] op_sel_hi:[1,0]
	v_mov_b32_e32 v34, v181
	v_mov_b32_e32 v35, v181
	v_cvt_pk_fp8_f32 v34, v30, v31
	v_cvt_pk_fp8_f32 v35, v32, v33
	v_pk_mul_f32 v[30:31], v[110:111], s[30:31] op_sel_hi:[1,0]
	v_pk_mul_f32 v[32:33], v[118:119], s[30:31] op_sel_hi:[1,0]
	v_add_u32_e32 v28, 48, v18
	v_cvt_pk_fp8_f32 v34, v30, v31 op_sel:[0,0,1]
	v_cvt_pk_fp8_f32 v35, v32, v33 op_sel:[0,0,1]
	v_pk_mul_f32 v[30:31], v[148:149], s[30:31] op_sel_hi:[1,0]
	v_pk_mul_f32 v[32:33], v[156:157], s[30:31] op_sel_hi:[1,0]
	v_mov_b32_e32 v36, v181
	v_mov_b32_e32 v37, v181
	v_ashrrev_i32_e32 v29, 31, v28
	v_cvt_pk_fp8_f32 v36, v30, v31
	v_cvt_pk_fp8_f32 v37, v32, v33
	v_lshlrev_b64 v[28:29], 11, v[28:29]
	ds_read_b128 v[24:27], v22
	v_lshl_add_u64 v[28:29], s[20:21], 0, v[28:29]
	v_lshl_add_u64 v[28:29], v[28:29], 0, s[6:7]
	v_pk_mul_f32 v[30:31], v[150:151], s[30:31] op_sel_hi:[1,0]
	v_pk_mul_f32 v[32:33], v[158:159], s[30:31] op_sel_hi:[1,0]
	v_lshl_add_u64 v[28:29], v[28:29], 0, v[180:181]
	v_cvt_pk_fp8_f32 v36, v30, v31 op_sel:[0,0,1]
	v_cvt_pk_fp8_f32 v37, v32, v33 op_sel:[0,0,1]
	v_lshl_add_u64 v[28:29], v[28:29], 0, s[18:19]
	v_lshl_add_u64 v[28:29], v[28:29], 0, v[20:21]
	s_waitcnt lgkmcnt(0)
	global_store_dwordx4 v[28:29], v[24:27], off nt
	ds_write_b64 v17, v[34:35]
	ds_write_b64 v17, v[36:37] offset:32
	v_pk_mul_f32 v[30:31], v[88:89], s[30:31] op_sel_hi:[1,0]
	v_pk_mul_f32 v[32:33], v[92:93], s[30:31] op_sel_hi:[1,0]
	v_mov_b32_e32 v34, v181
	v_mov_b32_e32 v35, v181
	v_cvt_pk_fp8_f32 v34, v30, v31
	v_cvt_pk_fp8_f32 v35, v32, v33
	v_pk_mul_f32 v[30:31], v[90:91], s[30:31] op_sel_hi:[1,0]
	v_pk_mul_f32 v[32:33], v[94:95], s[30:31] op_sel_hi:[1,0]
	v_add_u32_e32 v28, 0x80, v18
	v_cvt_pk_fp8_f32 v34, v30, v31 op_sel:[0,0,1]
	v_cvt_pk_fp8_f32 v35, v32, v33 op_sel:[0,0,1]
	v_pk_mul_f32 v[30:31], v[56:57], s[30:31] op_sel_hi:[1,0]
	v_pk_mul_f32 v[32:33], v[60:61], s[30:31] op_sel_hi:[1,0]
	v_mov_b32_e32 v36, v181
	v_mov_b32_e32 v37, v181
	v_ashrrev_i32_e32 v29, 31, v28
	v_cvt_pk_fp8_f32 v36, v30, v31
	v_cvt_pk_fp8_f32 v37, v32, v33
	v_lshlrev_b64 v[28:29], 11, v[28:29]
	ds_read_b128 v[24:27], v22
	v_lshl_add_u64 v[28:29], s[20:21], 0, v[28:29]
	v_lshl_add_u64 v[28:29], v[28:29], 0, s[6:7]
	v_pk_mul_f32 v[30:31], v[58:59], s[30:31] op_sel_hi:[1,0]
	v_pk_mul_f32 v[32:33], v[62:63], s[30:31] op_sel_hi:[1,0]
	v_lshl_add_u64 v[28:29], v[28:29], 0, v[180:181]
	v_cvt_pk_fp8_f32 v36, v30, v31 op_sel:[0,0,1]
	v_cvt_pk_fp8_f32 v37, v32, v33 op_sel:[0,0,1]
	v_lshl_add_u64 v[28:29], v[28:29], 0, s[18:19]
	v_lshl_add_u64 v[28:29], v[28:29], 0, v[20:21]
	s_waitcnt lgkmcnt(0)
	global_store_dwordx4 v[28:29], v[24:27], off nt
	ds_write_b64 v17, v[34:35]
	ds_write_b64 v17, v[36:37] offset:32
	v_pk_mul_f32 v[30:31], v[72:73], s[30:31] op_sel_hi:[1,0]
	v_mov_b32_e32 v34, v181
	v_cvt_pk_fp8_f32 v34, v30, v31
	v_add_u32_e32 v28, 0x90, v18
	v_ashrrev_i32_e32 v29, 31, v28
	v_pk_mul_f32 v[30:31], v[74:75], s[30:31] op_sel_hi:[1,0]
	v_lshlrev_b64 v[28:29], 11, v[28:29]
	v_cvt_pk_fp8_f32 v34, v30, v31 op_sel:[0,0,1]
	v_pk_mul_f32 v[8:9], v[8:9], s[30:31] op_sel_hi:[1,0]
	v_mov_b32_e32 v30, v181
	ds_read_b128 v[24:27], v22
	v_lshl_add_u64 v[28:29], s[20:21], 0, v[28:29]
	v_cvt_pk_fp8_f32 v30, v8, v9
	v_lshl_add_u64 v[28:29], v[28:29], 0, s[6:7]
	v_lshl_add_u64 v[28:29], v[28:29], 0, v[180:181]
	v_lshl_add_u64 v[28:29], v[28:29], 0, s[18:19]
	v_pk_mul_f32 v[32:33], v[76:77], s[30:31] op_sel_hi:[1,0]
	v_mov_b32_e32 v35, v181
	v_pk_mul_f32 v[8:9], v[10:11], s[30:31] op_sel_hi:[1,0]
	v_cvt_pk_fp8_f32 v35, v32, v33
	v_pk_mul_f32 v[12:13], v[12:13], s[30:31] op_sel_hi:[1,0]
	v_mov_b32_e32 v31, v181
	v_cvt_pk_fp8_f32 v30, v8, v9 op_sel:[0,0,1]
	v_lshl_add_u64 v[8:9], v[28:29], 0, v[20:21]
	v_cvt_pk_fp8_f32 v31, v12, v13
	v_pk_mul_f32 v[10:11], v[14:15], s[30:31] op_sel_hi:[1,0]
	s_waitcnt lgkmcnt(0)
	global_store_dwordx4 v[8:9], v[24:27], off nt
	v_pk_mul_f32 v[14:15], v[68:69], s[30:31] op_sel_hi:[1,0]
	v_pk_mul_f32 v[32:33], v[78:79], s[30:31] op_sel_hi:[1,0]
	v_mov_b32_e32 v26, v181
	v_cvt_pk_fp8_f32 v26, v14, v15
	v_cvt_pk_fp8_f32 v35, v32, v33 op_sel:[0,0,1]
	v_cvt_pk_fp8_f32 v31, v10, v11 op_sel:[0,0,1]
	v_pk_mul_f32 v[24:25], v[64:65], s[30:31] op_sel_hi:[1,0]
	v_mov_b32_e32 v27, v181
	v_pk_mul_f32 v[14:15], v[70:71], s[30:31] op_sel_hi:[1,0]
	v_add_u32_e32 v12, 0xa0, v18
	v_cvt_pk_fp8_f32 v27, v24, v25
	v_cvt_pk_fp8_f32 v26, v14, v15 op_sel:[0,0,1]
	v_pk_mul_f32 v[4:5], v[4:5], s[30:31] op_sel_hi:[1,0]
	v_pk_mul_f32 v[0:1], v[0:1], s[30:31] op_sel_hi:[1,0]
	v_mov_b32_e32 v14, v181
	v_mov_b32_e32 v15, v181
	v_ashrrev_i32_e32 v13, 31, v12
	v_cvt_pk_fp8_f32 v14, v4, v5
	v_cvt_pk_fp8_f32 v15, v0, v1
	ds_write_b64 v17, v[34:35]
	ds_write_b64 v17, v[30:31] offset:32
	v_lshlrev_b64 v[12:13], 11, v[12:13]
	ds_read_b128 v[8:11], v22
	v_lshl_add_u64 v[12:13], s[20:21], 0, v[12:13]
	v_pk_mul_f32 v[24:25], v[66:67], s[30:31] op_sel_hi:[1,0]
	v_lshl_add_u64 v[12:13], v[12:13], 0, s[6:7]
	v_cvt_pk_fp8_f32 v27, v24, v25 op_sel:[0,0,1]
	v_pk_mul_f32 v[0:1], v[6:7], s[30:31] op_sel_hi:[1,0]
	v_pk_mul_f32 v[2:3], v[2:3], s[30:31] op_sel_hi:[1,0]
	v_lshl_add_u64 v[12:13], v[12:13], 0, v[180:181]
	v_cvt_pk_fp8_f32 v14, v0, v1 op_sel:[0,0,1]
	v_cvt_pk_fp8_f32 v15, v2, v3 op_sel:[0,0,1]
	v_lshl_add_u64 v[12:13], v[12:13], 0, s[18:19]
	v_add_u32_e32 v4, 0xb0, v18
	v_lshl_add_u64 v[0:1], v[12:13], 0, v[20:21]
	v_ashrrev_i32_e32 v5, 31, v4
	s_waitcnt lgkmcnt(0)
	global_store_dwordx4 v[0:1], v[8:11], off nt
	ds_write_b64 v17, v[26:27]
	ds_write_b64 v17, v[14:15] offset:32
	v_lshlrev_b64 v[4:5], 11, v[4:5]
	ds_read_b128 v[0:3], v22
	v_lshl_add_u64 v[4:5], s[20:21], 0, v[4:5]
	v_lshl_add_u64 v[4:5], v[4:5], 0, s[6:7]
	v_lshl_add_u64 v[4:5], v[4:5], 0, v[180:181]
	v_lshl_add_u64 v[4:5], v[4:5], 0, s[18:19]
	v_lshl_add_u64 v[4:5], v[4:5], 0, v[20:21]
	s_mov_b64 s[6:7], -1
	s_andn2_b64 vcc, exec, s[4:5]
	s_mov_b32 s44, s36
	s_mov_b32 s42, s34
	s_mov_b64 s[48:49], s[40:41]
	s_mov_b64 s[50:51], s[38:39]
	s_waitcnt lgkmcnt(0)
	global_store_dwordx4 v[4:5], v[0:3], off nt
	s_cbranch_vccz .LBB0_1488

.LBB0_2750:
	v_mov_b32_e32 v17, v186
	v_mov_b32_e32 v19, v187
	s_nop 15
	s_nop 15
	v_pk_mul_f32 v[24:25], v[140:141], s[30:31] op_sel_hi:[1,0]
	v_lshl_add_u32 v18, v17, 4, v19
	v_ashrrev_i32_e32 v18, 2, v18
	v_and_b32_e32 v20, 3, v19
	v_mul_lo_u32 v21, v19, s71
	v_lshlrev_b32_e32 v17, 3, v17
	v_add3_u32 v17, s68, v21, v17
	v_mul_lo_u32 v21, v18, s71
	v_lshlrev_b32_e32 v20, 4, v20
	v_add3_u32 v22, s68, v21, v20
	v_lshlrev_b32_e32 v20, 6, v19
	v_and_b32_e32 v180, 0x80, v20
	v_pk_mul_f32 v[20:21], v[136:137], s[30:31] op_sel_hi:[1,0]
	v_mov_b32_e32 v26, v181
	v_mov_b32_e32 v27, v181
	v_cvt_pk_fp8_f32 v26, v20, v21
	v_cvt_pk_fp8_f32 v27, v24, v25
	v_pk_mul_f32 v[20:21], v[138:139], s[30:31] op_sel_hi:[1,0]
	v_pk_mul_f32 v[24:25], v[142:143], s[30:31] op_sel_hi:[1,0]
	v_cvt_pk_fp8_f32 v26, v20, v21 op_sel:[0,0,1]
	v_cvt_pk_fp8_f32 v27, v24, v25 op_sel:[0,0,1]
	v_pk_mul_f32 v[20:21], v[160:161], s[30:31] op_sel_hi:[1,0]
	v_pk_mul_f32 v[24:25], v[164:165], s[30:31] op_sel_hi:[1,0]
	v_mov_b32_e32 v28, v181
	v_mov_b32_e32 v29, v181
	v_cvt_pk_fp8_f32 v28, v20, v21
	v_cvt_pk_fp8_f32 v29, v24, v25
	v_pk_mul_f32 v[30:31], v[120:121], s[30:31] op_sel_hi:[1,0]
	v_pk_mul_f32 v[32:33], v[124:125], s[30:31] op_sel_hi:[1,0]
	v_mov_b32_e32 v34, v181
	v_mov_b32_e32 v35, v181
	v_cvt_pk_fp8_f32 v34, v30, v31
	v_cvt_pk_fp8_f32 v35, v32, v33
	s_lshl_b32 s6, s42, 8
	v_pk_mul_f32 v[20:21], v[162:163], s[30:31] op_sel_hi:[1,0]
	v_pk_mul_f32 v[24:25], v[166:167], s[30:31] op_sel_hi:[1,0]
	s_add_i32 s6, s6, s65
	v_cvt_pk_fp8_f32 v28, v20, v21 op_sel:[0,0,1]
	v_cvt_pk_fp8_f32 v29, v24, v25 op_sel:[0,0,1]
	v_pk_mul_f32 v[30:31], v[122:123], s[30:31] op_sel_hi:[1,0]
	v_pk_mul_f32 v[32:33], v[126:127], s[30:31] op_sel_hi:[1,0]
	v_add_u32_e32 v18, s6, v18
	v_lshlrev_b32_e32 v19, 4, v19
	v_cvt_pk_fp8_f32 v34, v30, v31 op_sel:[0,0,1]
	v_cvt_pk_fp8_f32 v35, v32, v33 op_sel:[0,0,1]
	v_pk_mul_f32 v[30:31], v[144:145], s[30:31] op_sel_hi:[1,0]
	v_pk_mul_f32 v[32:33], v[152:153], s[30:31] op_sel_hi:[1,0]
	v_mov_b32_e32 v36, v181
	v_mov_b32_e32 v37, v181
	v_and_b32_e32 v20, 16, v19
	v_ashrrev_i32_e32 v19, 31, v18
	v_cvt_pk_fp8_f32 v36, v30, v31
	v_cvt_pk_fp8_f32 v37, v32, v33
	s_lshl_b32 s6, s44, 8
	ds_write_b64 v17, v[26:27]
	ds_write_b64 v17, v[28:29] offset:32
	v_lshlrev_b64 v[28:29], 11, v[18:19]
	s_ashr_i32 s7, s6, 31
	ds_read_b128 v[24:27], v22
	v_lshl_add_u64 v[28:29], s[20:21], 0, v[28:29]
	v_lshl_add_u64 v[28:29], v[28:29], 0, s[6:7]
	v_pk_mul_f32 v[30:31], v[146:147], s[30:31] op_sel_hi:[1,0]
	v_pk_mul_f32 v[32:33], v[154:155], s[30:31] op_sel_hi:[1,0]
	v_lshl_add_u64 v[28:29], v[28:29], 0, v[180:181]
	v_cvt_pk_fp8_f32 v36, v30, v31 op_sel:[0,0,1]
	v_cvt_pk_fp8_f32 v37, v32, v33 op_sel:[0,0,1]
	v_mov_b32_e32 v21, v181
	v_lshl_add_u64 v[28:29], v[28:29], 0, s[18:19]
	v_lshl_add_u64 v[28:29], v[28:29], 0, v[20:21]
	s_waitcnt lgkmcnt(0)
	global_store_dwordx4 v[28:29], v[24:27], off nt
	ds_write_b64 v17, v[34:35]
	ds_write_b64 v17, v[36:37] offset:32
	v_pk_mul_f32 v[30:31], v[96:97], s[30:31] op_sel_hi:[1,0]
	v_pk_mul_f32 v[32:33], v[100:101], s[30:31] op_sel_hi:[1,0]
	v_mov_b32_e32 v34, v181
	v_mov_b32_e32 v35, v181
	v_cvt_pk_fp8_f32 v34, v30, v31
	v_cvt_pk_fp8_f32 v35, v32, v33
	v_pk_mul_f32 v[30:31], v[98:99], s[30:31] op_sel_hi:[1,0]
	v_pk_mul_f32 v[32:33], v[102:103], s[30:31] op_sel_hi:[1,0]
	v_add_u32_e32 v28, 16, v18
	v_cvt_pk_fp8_f32 v34, v30, v31 op_sel:[0,0,1]
	v_cvt_pk_fp8_f32 v35, v32, v33 op_sel:[0,0,1]
	v_pk_mul_f32 v[30:31], v[128:129], s[30:31] op_sel_hi:[1,0]
	v_pk_mul_f32 v[32:33], v[132:133], s[30:31] op_sel_hi:[1,0]
	v_mov_b32_e32 v36, v181
	v_mov_b32_e32 v37, v181
	v_ashrrev_i32_e32 v29, 31, v28
	v_cvt_pk_fp8_f32 v36, v30, v31
	v_cvt_pk_fp8_f32 v37, v32, v33
	v_lshlrev_b64 v[28:29], 11, v[28:29]
	ds_read_b128 v[24:27], v22
	v_lshl_add_u64 v[28:29], s[20:21], 0, v[28:29]
	v_lshl_add_u64 v[28:29], v[28:29], 0, s[6:7]
	v_pk_mul_f32 v[30:31], v[130:131], s[30:31] op_sel_hi:[1,0]
	v_pk_mul_f32 v[32:33], v[134:135], s[30:31] op_sel_hi:[1,0]
	v_lshl_add_u64 v[28:29], v[28:29], 0, v[180:181]
	v_cvt_pk_fp8_f32 v36, v30, v31 op_sel:[0,0,1]
	v_cvt_pk_fp8_f32 v37, v32, v33 op_sel:[0,0,1]
	v_lshl_add_u64 v[28:29], v[28:29], 0, s[18:19]
	v_lshl_add_u64 v[28:29], v[28:29], 0, v[20:21]
	s_waitcnt lgkmcnt(0)
	global_store_dwordx4 v[28:29], v[24:27], off nt
	ds_write_b64 v17, v[34:35]
	ds_write_b64 v17, v[36:37] offset:32
	v_pk_mul_f32 v[30:31], v[80:81], s[30:31] op_sel_hi:[1,0]
	v_pk_mul_f32 v[32:33], v[84:85], s[30:31] op_sel_hi:[1,0]
	v_mov_b32_e32 v34, v181
	v_mov_b32_e32 v35, v181
	v_cvt_pk_fp8_f32 v34, v30, v31
	v_cvt_pk_fp8_f32 v35, v32, v33
	v_pk_mul_f32 v[30:31], v[82:83], s[30:31] op_sel_hi:[1,0]
	v_pk_mul_f32 v[32:33], v[86:87], s[30:31] op_sel_hi:[1,0]
	v_add_u32_e32 v28, 32, v18
	v_cvt_pk_fp8_f32 v34, v30, v31 op_sel:[0,0,1]
	v_cvt_pk_fp8_f32 v35, v32, v33 op_sel:[0,0,1]
	v_pk_mul_f32 v[30:31], v[104:105], s[30:31] op_sel_hi:[1,0]
	v_pk_mul_f32 v[32:33], v[112:113], s[30:31] op_sel_hi:[1,0]
	v_mov_b32_e32 v36, v181
	v_mov_b32_e32 v37, v181
	v_ashrrev_i32_e32 v29, 31, v28
	v_cvt_pk_fp8_f32 v36, v30, v31
	v_cvt_pk_fp8_f32 v37, v32, v33
	v_lshlrev_b64 v[28:29], 11, v[28:29]
	ds_read_b128 v[24:27], v22
	v_lshl_add_u64 v[28:29], s[20:21], 0, v[28:29]
	v_lshl_add_u64 v[28:29], v[28:29], 0, s[6:7]
	v_pk_mul_f32 v[30:31], v[106:107], s[30:31] op_sel_hi:[1,0]
	v_pk_mul_f32 v[32:33], v[114:115], s[30:31] op_sel_hi:[1,0]
	v_lshl_add_u64 v[28:29], v[28:29], 0, v[180:181]
	v_cvt_pk_fp8_f32 v36, v30, v31 op_sel:[0,0,1]
	v_cvt_pk_fp8_f32 v37, v32, v33 op_sel:[0,0,1]
	v_lshl_add_u64 v[28:29], v[28:29], 0, s[18:19]
	v_lshl_add_u64 v[28:29], v[28:29], 0, v[20:21]
	s_waitcnt lgkmcnt(0)
	global_store_dwordx4 v[28:29], v[24:27], off nt
	ds_write_b64 v17, v[34:35]
	ds_write_b64 v17, v[36:37] offset:32
	v_pk_mul_f32 v[30:31], v[108:109], s[30:31] op_sel_hi:[1,0]
	v_pk_mul_f32 v[32:33], v[116:117], s[30:31] op_sel_hi:[1,0]
	v_mov_b32_e32 v34, v181
	v_mov_b32_e32 v35, v181
	v_cvt_pk_fp8_f32 v34, v30, v31
	v_cvt_pk_fp8_f32 v35, v32, v33
	v_pk_mul_f32 v[30:31], v[110:111], s[30:31] op_sel_hi:[1,0]
	v_pk_mul_f32 v[32:33], v[118:119], s[30:31] op_sel_hi:[1,0]
	v_add_u32_e32 v28, 48, v18
	v_cvt_pk_fp8_f32 v34, v30, v31 op_sel:[0,0,1]
	v_cvt_pk_fp8_f32 v35, v32, v33 op_sel:[0,0,1]
	v_pk_mul_f32 v[30:31], v[148:149], s[30:31] op_sel_hi:[1,0]
	v_pk_mul_f32 v[32:33], v[156:157], s[30:31] op_sel_hi:[1,0]
	v_mov_b32_e32 v36, v181
	v_mov_b32_e32 v37, v181
	v_ashrrev_i32_e32 v29, 31, v28
	v_cvt_pk_fp8_f32 v36, v30, v31
	v_cvt_pk_fp8_f32 v37, v32, v33
	v_lshlrev_b64 v[28:29], 11, v[28:29]
	ds_read_b128 v[24:27], v22
	v_lshl_add_u64 v[28:29], s[20:21], 0, v[28:29]
	v_lshl_add_u64 v[28:29], v[28:29], 0, s[6:7]
	v_pk_mul_f32 v[30:31], v[150:151], s[30:31] op_sel_hi:[1,0]
	v_pk_mul_f32 v[32:33], v[158:159], s[30:31] op_sel_hi:[1,0]
	v_lshl_add_u64 v[28:29], v[28:29], 0, v[180:181]
	v_cvt_pk_fp8_f32 v36, v30, v31 op_sel:[0,0,1]
	v_cvt_pk_fp8_f32 v37, v32, v33 op_sel:[0,0,1]
	v_lshl_add_u64 v[28:29], v[28:29], 0, s[18:19]
	v_lshl_add_u64 v[28:29], v[28:29], 0, v[20:21]
	s_waitcnt lgkmcnt(0)
	global_store_dwordx4 v[28:29], v[24:27], off nt
	ds_write_b64 v17, v[34:35]
	ds_write_b64 v17, v[36:37] offset:32
	v_pk_mul_f32 v[30:31], v[88:89], s[30:31] op_sel_hi:[1,0]
	v_pk_mul_f32 v[32:33], v[92:93], s[30:31] op_sel_hi:[1,0]
	v_mov_b32_e32 v34, v181
	v_mov_b32_e32 v35, v181
	v_cvt_pk_fp8_f32 v34, v30, v31
	v_cvt_pk_fp8_f32 v35, v32, v33
	v_pk_mul_f32 v[30:31], v[90:91], s[30:31] op_sel_hi:[1,0]
	v_pk_mul_f32 v[32:33], v[94:95], s[30:31] op_sel_hi:[1,0]
	v_add_u32_e32 v28, 0x80, v18
	v_cvt_pk_fp8_f32 v34, v30, v31 op_sel:[0,0,1]
	v_cvt_pk_fp8_f32 v35, v32, v33 op_sel:[0,0,1]
	v_pk_mul_f32 v[30:31], v[56:57], s[30:31] op_sel_hi:[1,0]
	v_pk_mul_f32 v[32:33], v[60:61], s[30:31] op_sel_hi:[1,0]
	v_mov_b32_e32 v36, v181
	v_mov_b32_e32 v37, v181
	v_ashrrev_i32_e32 v29, 31, v28
	v_cvt_pk_fp8_f32 v36, v30, v31
	v_cvt_pk_fp8_f32 v37, v32, v33
	v_lshlrev_b64 v[28:29], 11, v[28:29]
	ds_read_b128 v[24:27], v22
	v_lshl_add_u64 v[28:29], s[20:21], 0, v[28:29]
	v_lshl_add_u64 v[28:29], v[28:29], 0, s[6:7]
	v_pk_mul_f32 v[30:31], v[58:59], s[30:31] op_sel_hi:[1,0]
	v_pk_mul_f32 v[32:33], v[62:63], s[30:31] op_sel_hi:[1,0]
	v_lshl_add_u64 v[28:29], v[28:29], 0, v[180:181]
	v_cvt_pk_fp8_f32 v36, v30, v31 op_sel:[0,0,1]
	v_cvt_pk_fp8_f32 v37, v32, v33 op_sel:[0,0,1]
	v_lshl_add_u64 v[28:29], v[28:29], 0, s[18:19]
	v_lshl_add_u64 v[28:29], v[28:29], 0, v[20:21]
	s_waitcnt lgkmcnt(0)
	global_store_dwordx4 v[28:29], v[24:27], off nt
	ds_write_b64 v17, v[34:35]
	ds_write_b64 v17, v[36:37] offset:32
	v_pk_mul_f32 v[30:31], v[72:73], s[30:31] op_sel_hi:[1,0]
	v_mov_b32_e32 v34, v181
	v_cvt_pk_fp8_f32 v34, v30, v31
	v_add_u32_e32 v28, 0x90, v18
	v_ashrrev_i32_e32 v29, 31, v28
	v_pk_mul_f32 v[30:31], v[74:75], s[30:31] op_sel_hi:[1,0]
	v_lshlrev_b64 v[28:29], 11, v[28:29]
	v_cvt_pk_fp8_f32 v34, v30, v31 op_sel:[0,0,1]
	v_pk_mul_f32 v[8:9], v[8:9], s[30:31] op_sel_hi:[1,0]
	v_mov_b32_e32 v30, v181
	ds_read_b128 v[24:27], v22
	v_lshl_add_u64 v[28:29], s[20:21], 0, v[28:29]
	v_cvt_pk_fp8_f32 v30, v8, v9
	v_lshl_add_u64 v[28:29], v[28:29], 0, s[6:7]
	v_lshl_add_u64 v[28:29], v[28:29], 0, v[180:181]
	v_lshl_add_u64 v[28:29], v[28:29], 0, s[18:19]
	v_pk_mul_f32 v[32:33], v[76:77], s[30:31] op_sel_hi:[1,0]
	v_mov_b32_e32 v35, v181
	v_pk_mul_f32 v[8:9], v[10:11], s[30:31] op_sel_hi:[1,0]
	v_cvt_pk_fp8_f32 v35, v32, v33
	v_pk_mul_f32 v[12:13], v[12:13], s[30:31] op_sel_hi:[1,0]
	v_mov_b32_e32 v31, v181
	v_cvt_pk_fp8_f32 v30, v8, v9 op_sel:[0,0,1]
	v_lshl_add_u64 v[8:9], v[28:29], 0, v[20:21]
	v_cvt_pk_fp8_f32 v31, v12, v13
	v_pk_mul_f32 v[10:11], v[14:15], s[30:31] op_sel_hi:[1,0]
	s_waitcnt lgkmcnt(0)
	global_store_dwordx4 v[8:9], v[24:27], off nt
	v_pk_mul_f32 v[14:15], v[68:69], s[30:31] op_sel_hi:[1,0]
	v_pk_mul_f32 v[32:33], v[78:79], s[30:31] op_sel_hi:[1,0]
	v_mov_b32_e32 v26, v181
	v_cvt_pk_fp8_f32 v26, v14, v15
	v_cvt_pk_fp8_f32 v35, v32, v33 op_sel:[0,0,1]
	v_cvt_pk_fp8_f32 v31, v10, v11 op_sel:[0,0,1]
	v_pk_mul_f32 v[24:25], v[64:65], s[30:31] op_sel_hi:[1,0]
	v_mov_b32_e32 v27, v181
	v_pk_mul_f32 v[14:15], v[70:71], s[30:31] op_sel_hi:[1,0]
	v_add_u32_e32 v12, 0xa0, v18
	v_cvt_pk_fp8_f32 v27, v24, v25
	v_cvt_pk_fp8_f32 v26, v14, v15 op_sel:[0,0,1]
	v_pk_mul_f32 v[4:5], v[4:5], s[30:31] op_sel_hi:[1,0]
	v_pk_mul_f32 v[0:1], v[0:1], s[30:31] op_sel_hi:[1,0]
	v_mov_b32_e32 v14, v181
	v_mov_b32_e32 v15, v181
	v_ashrrev_i32_e32 v13, 31, v12
	v_cvt_pk_fp8_f32 v14, v4, v5
	v_cvt_pk_fp8_f32 v15, v0, v1
	ds_write_b64 v17, v[34:35]
	ds_write_b64 v17, v[30:31] offset:32
	v_lshlrev_b64 v[12:13], 11, v[12:13]
	ds_read_b128 v[8:11], v22
	v_lshl_add_u64 v[12:13], s[20:21], 0, v[12:13]
	v_pk_mul_f32 v[24:25], v[66:67], s[30:31] op_sel_hi:[1,0]
	v_lshl_add_u64 v[12:13], v[12:13], 0, s[6:7]
	v_cvt_pk_fp8_f32 v27, v24, v25 op_sel:[0,0,1]
	v_pk_mul_f32 v[0:1], v[6:7], s[30:31] op_sel_hi:[1,0]
	v_pk_mul_f32 v[2:3], v[2:3], s[30:31] op_sel_hi:[1,0]
	v_lshl_add_u64 v[12:13], v[12:13], 0, v[180:181]
	v_cvt_pk_fp8_f32 v14, v0, v1 op_sel:[0,0,1]
	v_cvt_pk_fp8_f32 v15, v2, v3 op_sel:[0,0,1]
	v_lshl_add_u64 v[12:13], v[12:13], 0, s[18:19]
	v_add_u32_e32 v4, 0xb0, v18
	v_lshl_add_u64 v[0:1], v[12:13], 0, v[20:21]
	v_ashrrev_i32_e32 v5, 31, v4
	s_waitcnt lgkmcnt(0)
	global_store_dwordx4 v[0:1], v[8:11], off nt
	ds_write_b64 v17, v[26:27]
	ds_write_b64 v17, v[14:15] offset:32
	v_lshlrev_b64 v[4:5], 11, v[4:5]
	ds_read_b128 v[0:3], v22
	v_lshl_add_u64 v[4:5], s[20:21], 0, v[4:5]
	v_lshl_add_u64 v[4:5], v[4:5], 0, s[6:7]
	v_lshl_add_u64 v[4:5], v[4:5], 0, v[180:181]
	v_lshl_add_u64 v[4:5], v[4:5], 0, s[18:19]
	v_lshl_add_u64 v[4:5], v[4:5], 0, v[20:21]
	s_mov_b64 s[6:7], -1
	s_andn2_b64 vcc, exec, s[4:5]
	s_mov_b32 s44, s36
	s_mov_b32 s42, s34
	s_mov_b64 s[48:49], s[40:41]
	s_mov_b64 s[50:51], s[38:39]
	s_waitcnt lgkmcnt(0)
	global_store_dwordx4 v[4:5], v[0:3], off nt
	s_cbranch_vccz .LBB0_2765
